# G2: gemm1 next-unit token-row lookups issued exec-masked into loop-untouched registers with no wait in the unit header; row offsets formed after the K-loop's first counted wait (one-shot flag); on top
# speedup vs baseline: 1.0024x; 1.0002x over previous
.LBB0_1389:
	v_lshrrev_b32_e32 v10, 1, v0
	v_and_b32_e32 v10, 24, v10
	s_add_u32 s14, s14, 0x9e940000
	v_and_b32_e32 v1, 15, v0
	v_lshlrev_b32_e32 v11, 1, v10
	v_lshlrev_b32_e32 v0, 2, v0
	s_addc_u32 s15, s15, 0
	v_lshl_or_b32 v133, s0, 6, v1
	v_lshl_or_b32 v1, v1, 6, v11
	s_lshl_b32 s0, s0, 13
	v_and_b32_e32 v0, 32, v0
	v_bitop3_b32 v11, v1, s0, v0 bitop3:0xde
	s_lshl_b32 s0, s1, 5
	s_and_b32 s4, s0, 0x60
	s_lshl_b32 s0, s4, 7
	v_bitop3_b32 v135, s0, v1, v0 bitop3:0xf6
	s_add_i32 m0, s43, 0x18000
	v_lshl_add_u64 v[0:1], v[8:9], 0, s[94:95]
	s_waitcnt vmcnt(4)
	s_barrier
	global_load_lds_dwordx4 v[0:1], off
	v_lshl_add_u64 v[0:1], v[6:7], 0, s[94:95]
	s_add_i32 m0, s43, 0x1a000
	s_add_i32 s47, s43, 0x8000
	s_add_i32 s48, s43, 0xa000
	global_load_lds_dwordx4 v[0:1], off
	v_lshl_add_u64 v[0:1], v[2:3], 0, s[94:95]
	s_mov_b32 m0, s47
	s_add_u32 s0, s34, 0x80080
	global_load_lds_dwordx4 v[0:1], off
	v_lshl_add_u64 v[0:1], v[4:5], 0, s[94:95]
	s_mov_b32 m0, s48
	s_addc_u32 s1, s35, 0
	global_load_lds_dwordx4 v[0:1], off
	s_add_i32 m0, s43, 0x1c000
	v_lshl_add_u64 v[0:1], s[0:1], 0, v[130:131]
	global_load_lds_dwordx4 v[0:1], off
	v_lshl_add_u64 v[0:1], s[0:1], 0, v[136:137]
	s_add_i32 m0, s43, 0x1e000
	s_cmpk_lt_u32 s16, 0x100
	global_load_lds_dwordx4 v[0:1], off
	s_cselect_b64 s[16:17], -1, 0
	s_add_i32 s0, s2, 64
	s_ashr_i32 s1, s0, 31
	s_ashr_i32 s49, s40, 31
	s_lshl_b64 s[18:19], s[0:1], 2
	s_and_b32 s5, s40, 7
	s_ashr_i32 s50, s40, 3
	s_ashr_i32 s22, s0, 3
	s_and_b32 s23, s2, 7
	s_cmp_lt_u32 s5, s23
	s_cselect_b64 s[0:1], -1, 0
	s_cmp_lg_u64 s[0:1], 0
	s_addc_u32 s0, s22, 0
	s_waitcnt vmcnt(6)
	s_ashr_i32 s1, s0, 31
	v_lshl_add_u32 v154, v146, 12, v150
	v_lshl_add_u32 v155, v147, 12, v151
	s_lshl_b64 s[20:21], s[0:1], 2
	s_mul_i32 s52, s22, s5
	s_min_u32 s0, s5, s23
	v_mov_b32_e32 v0, 0
	v_add_u32_e32 v153, 0x80000, v154
	v_add_u32_e32 v156, 0x80000, v155
	s_mov_b32 s54, 0
	s_ashr_i32 s51, s50, 31
	s_add_i32 s52, s52, s0
	v_add_u32_e32 v152, 0, v11
	s_lshl_b32 s84, s4, 1
	v_lshlrev_b32_e32 v140, 1, v10
	s_mov_b64 s[26:27], s[6:7]
	v_mov_b32_e32 v1, v0
	v_mov_b32_e32 v2, v0
	v_mov_b32_e32 v3, v0
	v_mov_b32_e32 v4, v0
	v_mov_b32_e32 v5, v0
	v_mov_b32_e32 v6, v0
	v_mov_b32_e32 v7, v0
	v_mov_b32_e32 v8, v0
	v_mov_b32_e32 v9, v0
	v_mov_b32_e32 v10, v0
	v_mov_b32_e32 v11, v0
	v_mov_b32_e32 v12, v0
	v_mov_b32_e32 v13, v0
	v_mov_b32_e32 v14, v0
	v_mov_b32_e32 v15, v0
	v_mov_b32_e32 v16, v0
	v_mov_b32_e32 v17, v0
	v_mov_b32_e32 v18, v0
	v_mov_b32_e32 v19, v0
	v_mov_b32_e32 v20, v0
	v_mov_b32_e32 v21, v0
	v_mov_b32_e32 v22, v0
	v_mov_b32_e32 v23, v0
	v_mov_b32_e32 v24, v0
	v_mov_b32_e32 v25, v0
	v_mov_b32_e32 v26, v0
	v_mov_b32_e32 v27, v0
	v_mov_b32_e32 v28, v0
	v_mov_b32_e32 v29, v0
	v_mov_b32_e32 v30, v0
	v_mov_b32_e32 v31, v0
	v_mov_b32_e32 v32, v0
	v_mov_b32_e32 v33, v0
	v_mov_b32_e32 v34, v0
	v_mov_b32_e32 v35, v0
	v_mov_b32_e32 v36, v0
	v_mov_b32_e32 v37, v0
	v_mov_b32_e32 v38, v0
	v_mov_b32_e32 v39, v0
	v_mov_b32_e32 v40, v0
	v_mov_b32_e32 v41, v0
	v_mov_b32_e32 v42, v0
	v_mov_b32_e32 v43, v0
	v_mov_b32_e32 v44, v0
	v_mov_b32_e32 v45, v0
	v_mov_b32_e32 v46, v0
	v_mov_b32_e32 v47, v0
	v_mov_b32_e32 v48, v0
	v_mov_b32_e32 v49, v0
	v_mov_b32_e32 v50, v0
	v_mov_b32_e32 v51, v0
	v_mov_b32_e32 v52, v0
	v_mov_b32_e32 v53, v0
	v_mov_b32_e32 v54, v0
	v_mov_b32_e32 v55, v0
	v_mov_b32_e32 v56, v0
	v_mov_b32_e32 v57, v0
	v_mov_b32_e32 v58, v0
	v_mov_b32_e32 v59, v0
	v_mov_b32_e32 v60, v0
	v_mov_b32_e32 v61, v0
	v_mov_b32_e32 v62, v0
	v_mov_b32_e32 v63, v0
	v_mov_b32_e32 v64, v0
	v_mov_b32_e32 v65, v0
	v_mov_b32_e32 v66, v0
	v_mov_b32_e32 v67, v0
	v_mov_b32_e32 v68, v0
	v_mov_b32_e32 v69, v0
	v_mov_b32_e32 v70, v0
	v_mov_b32_e32 v71, v0
	v_mov_b32_e32 v72, v0
	v_mov_b32_e32 v73, v0
	v_mov_b32_e32 v74, v0
	v_mov_b32_e32 v75, v0
	v_mov_b32_e32 v76, v0
	v_mov_b32_e32 v77, v0
	v_mov_b32_e32 v78, v0
	v_mov_b32_e32 v79, v0
	v_mov_b32_e32 v80, v0
	v_mov_b32_e32 v81, v0
	v_mov_b32_e32 v82, v0
	v_mov_b32_e32 v83, v0
	v_mov_b32_e32 v84, v0
	v_mov_b32_e32 v85, v0
	v_mov_b32_e32 v86, v0
	v_mov_b32_e32 v87, v0
	v_mov_b32_e32 v88, v0
	v_mov_b32_e32 v89, v0
	v_mov_b32_e32 v90, v0
	v_mov_b32_e32 v91, v0
	v_mov_b32_e32 v92, v0
	v_mov_b32_e32 v93, v0
	v_mov_b32_e32 v94, v0
	v_mov_b32_e32 v95, v0
	v_mov_b32_e32 v96, v0
	v_mov_b32_e32 v97, v0
	v_mov_b32_e32 v98, v0
	v_mov_b32_e32 v99, v0
	v_mov_b32_e32 v100, v0
	v_mov_b32_e32 v101, v0
	v_mov_b32_e32 v102, v0
	v_mov_b32_e32 v103, v0
	v_mov_b32_e32 v104, v0
	v_mov_b32_e32 v105, v0
	v_mov_b32_e32 v106, v0
	v_mov_b32_e32 v107, v0
	v_mov_b32_e32 v108, v0
	v_mov_b32_e32 v109, v0
	v_mov_b32_e32 v110, v0
	v_mov_b32_e32 v111, v0
	v_mov_b32_e32 v112, v0
	v_mov_b32_e32 v113, v0
	v_mov_b32_e32 v114, v0
	v_mov_b32_e32 v115, v0
	v_mov_b32_e32 v116, v0
	v_mov_b32_e32 v117, v0
	v_mov_b32_e32 v118, v0
	v_mov_b32_e32 v119, v0
	v_mov_b32_e32 v120, v0
	v_mov_b32_e32 v121, v0
	v_mov_b32_e32 v122, v0
	v_mov_b32_e32 v123, v0
	v_mov_b32_e32 v124, v0
	v_mov_b32_e32 v125, v0
	v_mov_b32_e32 v126, v0
	v_mov_b32_e32 v127, v0
	s_barrier
	s_mov_b32 s92, 0
	s_branch .LBB0_1391

.LG1_gather:
	s_ashr_i32 s36, s53, 8
	s_lshl_b32 s36, s36, 2
	s_add_i32 s36, s36, 0x25200
	v_mov_b32_e32 v208, s36
	ds_read_b32 v208, v208
	s_waitcnt lgkmcnt(0)
	v_lshlrev_b32_e32 v210, 2, v208
	v_add_u32_e32 v211, 0x25000, v210
	ds_read_b32 v211, v211
	v_add_u32_e32 v210, 0x25c80, v210
	ds_read_b32 v210, v210
	v_ashrrev_i32_e32 v209, 31, v208
	v_lshlrev_b64 v[208:209], 16, v[208:209]
	v_lshl_add_u64 v[208:209], s[10:11], 0, v[208:209]
	s_waitcnt lgkmcnt(0)
	v_sub_u32_e32 v211, s53, v211
	v_add_u32_e32 v212, v211, v146
	v_add_u32_e32 v214, v211, v147
	v_add_u32_e32 v216, v211, v148
	v_add_u32_e32 v218, v211, v149
	v_cmp_lt_i32_e64 s[36:37], v212, v210
	v_cmp_lt_i32_e64 s[38:39], v214, v210
	v_cmp_lt_i32_e64 s[58:59], v216, v210
	v_cmp_lt_i32_e64 s[60:61], v218, v210
	v_ashrrev_i32_e32 v213, 31, v212
	v_ashrrev_i32_e32 v215, 31, v214
	v_ashrrev_i32_e32 v217, 31, v216
	v_ashrrev_i32_e32 v219, 31, v218
	v_lshl_add_u64 v[212:213], v[212:213], 2, v[208:209]
	v_lshl_add_u64 v[214:215], v[214:215], 2, v[208:209]
	v_lshl_add_u64 v[216:217], v[216:217], 2, v[208:209]
	v_lshl_add_u64 v[218:219], v[218:219], 2, v[208:209]
	v_mov_b32_e32 v157, 0
	v_mov_b32_e32 v207, 0
	v_mov_b32_e32 v148, 0
	v_mov_b32_e32 v149, 0
	s_mov_b64 exec, s[36:37]
	global_load_dword v157, v[212:213], off
	s_mov_b64 exec, s[38:39]
	global_load_dword v207, v[214:215], off
	s_mov_b64 exec, s[58:59]
	global_load_dword v148, v[216:217], off
	s_mov_b64 exec, s[60:61]
	global_load_dword v149, v[218:219], off
	s_mov_b64 exec, -1
	s_mov_b32 s92, 1
	s_branch .LG2_join

.LG2_join:
	s_mov_b64 s[30:31], s[6:7]
	s_mov_b64 s[4:5], s[24:25]

.LBB0_1423:
	s_add_u32 s36, s26, s34
	s_addc_u32 s37, s27, s35
	s_add_u32 s38, s36, 0x100
	s_addc_u32 s39, s37, 0
	s_add_u32 s58, s23, s34
	s_addc_u32 s59, s56, s35
	s_add_i32 s60, 0, 0x10000
	v_add_u32_e32 v141, s60, v135
	ds_read_b128 v[158:161], v141
	ds_read_b128 v[162:165], v141 offset:1024
	ds_read_b128 v[172:175], v141 offset:2048
	ds_read_b128 v[176:179], v141 offset:3072
	s_cmpk_eq_i32 s34, 0xf00
	s_cselect_b64 vcc, -1, 0
	s_and_b64 s[36:37], vcc, exec
	v_cndmask_b32_e32 v168, v134, v154, vcc
	v_cndmask_b32_e32 v166, v132, v155, vcc
	v_cndmask_b32_e32 v129, v128, v153, vcc
	v_cndmask_b32_e32 v139, v138, v156, vcc
	s_cselect_b32 s39, s31, s39
	s_cselect_b32 s38, s30, s38
	s_cselect_b32 s37, s5, s59
	s_cselect_b32 s36, s4, s58
	v_lshl_add_u64 v[184:185], v[144:145], 0, s[34:35]
	s_add_i32 m0, s43, 0xc000
	s_nop 0
	global_load_lds_dwordx4 v[184:185], off
	v_lshl_add_u64 v[184:185], v[142:143], 0, s[34:35]
	s_add_i32 m0, s43, 0xe000
	s_nop 0
	global_load_lds_dwordx4 v[184:185], off
	s_waitcnt lgkmcnt(0)
	s_setprio 1
	s_barrier
	s_waitcnt lgkmcnt(0)
	v_mfma_f32_16x16x32_bf16 v[124:127], v[158:161], v[180:183], v[124:127]
	v_mfma_f32_16x16x32_bf16 v[120:123], v[172:175], v[180:183], v[120:123]
	v_mfma_f32_16x16x32_bf16 v[116:119], v[158:161], v[212:215], v[116:119]
	v_mfma_f32_16x16x32_bf16 v[112:115], v[172:175], v[212:215], v[112:115]
	v_mfma_f32_16x16x32_bf16 v[108:111], v[158:161], v[220:223], v[108:111]
	v_mfma_f32_16x16x32_bf16 v[104:107], v[172:175], v[220:223], v[104:107]
	v_mfma_f32_16x16x32_bf16 v[100:103], v[158:161], v[228:231], v[100:103]
	v_mfma_f32_16x16x32_bf16 v[96:99], v[172:175], v[228:231], v[96:99]
	v_mfma_f32_16x16x32_bf16 v[124:127], v[162:165], v[208:211], v[124:127]
	v_mfma_f32_16x16x32_bf16 v[120:123], v[176:179], v[208:211], v[120:123]
	v_mfma_f32_16x16x32_bf16 v[116:119], v[162:165], v[216:219], v[116:119]
	v_mfma_f32_16x16x32_bf16 v[112:115], v[176:179], v[216:219], v[112:115]
	v_mfma_f32_16x16x32_bf16 v[108:111], v[162:165], v[224:227], v[108:111]
	v_mfma_f32_16x16x32_bf16 v[104:107], v[176:179], v[224:227], v[104:107]
	v_mfma_f32_16x16x32_bf16 v[100:103], v[162:165], v[232:235], v[100:103]
	v_mfma_f32_16x16x32_bf16 v[96:99], v[176:179], v[232:235], v[96:99]
	s_barrier
	s_setprio 0
	s_add_i32 s61, 0, 0x14000
	s_add_i32 s58, s60, s9
	v_add_u32_e32 v141, s61, v135
	v_lshl_add_u64 v[184:185], s[36:37], 0, v[130:131]
	s_mov_b32 m0, s58
	ds_read_b128 v[236:239], v141
	ds_read_b128 v[240:243], v141 offset:1024
	ds_read_b128 v[244:247], v141 offset:2048
	ds_read_b128 v[248:251], v141 offset:3072
	global_load_lds_dwordx4 v[184:185], off
	v_lshl_add_u64 v[188:189], s[36:37], 0, v[136:137]
	s_add_i32 m0, s58, 0x2000
	s_nop 0
	global_load_lds_dwordx4 v[188:189], off
	s_setprio 1
	s_barrier
	s_waitcnt lgkmcnt(0)
	v_mfma_f32_16x16x32_bf16 v[92:95], v[236:239], v[180:183], v[92:95]
	v_mfma_f32_16x16x32_bf16 v[88:91], v[244:247], v[180:183], v[88:91]
	ds_read_b128 v[180:183], v152 offset:16384
	v_mfma_f32_16x16x32_bf16 v[84:87], v[236:239], v[212:215], v[84:87]
	v_mfma_f32_16x16x32_bf16 v[80:83], v[244:247], v[212:215], v[80:83]
	ds_read_b128 v[212:215], v152 offset:18432
	v_mfma_f32_16x16x32_bf16 v[76:79], v[236:239], v[220:223], v[76:79]
	v_mfma_f32_16x16x32_bf16 v[72:75], v[244:247], v[220:223], v[72:75]
	ds_read_b128 v[220:223], v152 offset:20480
	v_mfma_f32_16x16x32_bf16 v[68:71], v[236:239], v[228:231], v[68:71]
	v_mfma_f32_16x16x32_bf16 v[64:67], v[244:247], v[228:231], v[64:67]
	ds_read_b128 v[228:231], v152 offset:22528
	v_mfma_f32_16x16x32_bf16 v[92:95], v[240:243], v[208:211], v[92:95]
	v_mfma_f32_16x16x32_bf16 v[88:91], v[248:251], v[208:211], v[88:91]
	ds_read_b128 v[208:211], v152 offset:17408
	v_mfma_f32_16x16x32_bf16 v[84:87], v[240:243], v[216:219], v[84:87]
	v_mfma_f32_16x16x32_bf16 v[80:83], v[248:251], v[216:219], v[80:83]
	ds_read_b128 v[216:219], v152 offset:19456
	v_mfma_f32_16x16x32_bf16 v[76:79], v[240:243], v[224:227], v[76:79]
	v_mfma_f32_16x16x32_bf16 v[72:75], v[248:251], v[224:227], v[72:75]
	ds_read_b128 v[224:227], v152 offset:21504
	v_mfma_f32_16x16x32_bf16 v[68:71], v[240:243], v[232:235], v[68:71]
	v_mfma_f32_16x16x32_bf16 v[64:67], v[248:251], v[232:235], v[64:67]
	ds_read_b128 v[232:235], v152 offset:23552
	s_barrier
	s_setprio 0
	s_mov_b32 m0, s43
	s_nop 0
	global_load_lds_dwordx4 v168, s[38:39]
	s_mov_b32 m0, s44
	v_mov_b32_e32 v167, v169
	global_load_lds_dwordx4 v166, s[38:39]
	s_waitcnt vmcnt(8)
	v_lshl_add_u64 v[170:171], s[38:39], 0, v[168:169]
	v_lshl_add_u64 v[166:167], s[38:39], 0, v[166:167]
	s_setprio 1
	s_barrier
	s_waitcnt lgkmcnt(0)
	v_mfma_f32_16x16x32_bf16 v[60:63], v[158:161], v[180:183], v[60:63]
	v_mfma_f32_16x16x32_bf16 v[56:59], v[172:175], v[180:183], v[56:59]
	v_mfma_f32_16x16x32_bf16 v[52:55], v[158:161], v[212:215], v[52:55]
	v_mfma_f32_16x16x32_bf16 v[48:51], v[172:175], v[212:215], v[48:51]
	v_mfma_f32_16x16x32_bf16 v[44:47], v[158:161], v[220:223], v[44:47]
	v_mfma_f32_16x16x32_bf16 v[40:43], v[172:175], v[220:223], v[40:43]
	v_mfma_f32_16x16x32_bf16 v[36:39], v[158:161], v[228:231], v[36:39]
	v_mfma_f32_16x16x32_bf16 v[32:35], v[172:175], v[228:231], v[32:35]
	v_mfma_f32_16x16x32_bf16 v[60:63], v[162:165], v[208:211], v[60:63]
	v_mfma_f32_16x16x32_bf16 v[56:59], v[176:179], v[208:211], v[56:59]
	v_mfma_f32_16x16x32_bf16 v[52:55], v[162:165], v[216:219], v[52:55]
	v_mfma_f32_16x16x32_bf16 v[48:51], v[176:179], v[216:219], v[48:51]
	v_mfma_f32_16x16x32_bf16 v[44:47], v[162:165], v[224:227], v[44:47]
	v_mfma_f32_16x16x32_bf16 v[40:43], v[176:179], v[224:227], v[40:43]
	v_mfma_f32_16x16x32_bf16 v[36:39], v[162:165], v[232:235], v[36:39]
	v_mfma_f32_16x16x32_bf16 v[32:35], v[176:179], v[232:235], v[32:35]
	s_barrier
	s_setprio 0
	s_add_u32 s58, s36, 0x80000
	s_addc_u32 s59, s37, 0
	s_add_i32 s60, s61, s9
	v_lshl_add_u64 v[158:159], s[58:59], 0, v[130:131]
	s_mov_b32 m0, s60
	s_nop 0
	global_load_lds_dwordx4 v[158:159], off
	v_lshl_add_u64 v[158:159], s[58:59], 0, v[136:137]
	s_add_i32 m0, s60, 0x2000
	s_nop 0
	global_load_lds_dwordx4 v[158:159], off
	s_waitcnt vmcnt(6)
	s_cmp_eq_u32 s92, 1
	s_cbranch_scc0 .LG2_skip
	v_lshl_add_u32 v153, v148, 12, v150
	v_lshl_add_u32 v155, v207, 12, v151
	v_lshl_add_u32 v154, v157, 12, v150
	v_lshl_add_u32 v156, v149, 12, v151
	v_add_u32_e32 v148, 0x80, v146
	v_add_u32_e32 v149, 0x80, v147
	s_mov_b32 s92, 0
.LG2_skip:
	s_setprio 1
	s_barrier
	v_mfma_f32_16x16x32_bf16 v[28:31], v[236:239], v[180:183], v[28:31]
	v_mfma_f32_16x16x32_bf16 v[24:27], v[244:247], v[180:183], v[24:27]
	ds_read_b128 v[180:183], v152 offset:32768
	v_mfma_f32_16x16x32_bf16 v[20:23], v[236:239], v[212:215], v[20:23]
	v_mfma_f32_16x16x32_bf16 v[16:19], v[244:247], v[212:215], v[16:19]
	ds_read_b128 v[212:215], v152 offset:34816
	v_mfma_f32_16x16x32_bf16 v[12:15], v[236:239], v[220:223], v[12:15]
	v_mfma_f32_16x16x32_bf16 v[8:11], v[244:247], v[220:223], v[8:11]
	ds_read_b128 v[220:223], v152 offset:36864
	v_mfma_f32_16x16x32_bf16 v[4:7], v[236:239], v[228:231], v[4:7]
	v_mfma_f32_16x16x32_bf16 v[0:3], v[244:247], v[228:231], v[0:3]
	ds_read_b128 v[228:231], v152 offset:38912
	v_mfma_f32_16x16x32_bf16 v[28:31], v[240:243], v[208:211], v[28:31]
	v_mfma_f32_16x16x32_bf16 v[24:27], v[248:251], v[208:211], v[24:27]
	ds_read_b128 v[208:211], v152 offset:33792
	v_mfma_f32_16x16x32_bf16 v[20:23], v[240:243], v[216:219], v[20:23]
	v_mfma_f32_16x16x32_bf16 v[16:19], v[248:251], v[216:219], v[16:19]
	ds_read_b128 v[216:219], v152 offset:35840
	v_mfma_f32_16x16x32_bf16 v[12:15], v[240:243], v[224:227], v[12:15]
	v_mfma_f32_16x16x32_bf16 v[8:11], v[248:251], v[224:227], v[8:11]
	ds_read_b128 v[224:227], v152 offset:37888
	v_mfma_f32_16x16x32_bf16 v[4:7], v[240:243], v[232:235], v[4:7]
	v_mfma_f32_16x16x32_bf16 v[0:3], v[248:251], v[232:235], v[0:3]
	ds_read_b128 v[232:235], v152 offset:39936
	s_barrier
	s_setprio 0
	s_add_i32 s58, 0, 0x18000
	v_add_u32_e32 v141, s58, v135
	ds_read_b128 v[158:161], v141
	ds_read_b128 v[162:165], v141 offset:1024
	ds_read_b128 v[172:175], v141 offset:2048
	ds_read_b128 v[176:179], v141 offset:3072
	s_mov_b32 m0, s45
	s_nop 0
	global_load_lds_dwordx4 v129, s[38:39]
	s_mov_b32 m0, s46
	s_nop 0
	global_load_lds_dwordx4 v139, s[38:39]
	s_waitcnt lgkmcnt(0)
	s_setprio 1
	s_barrier
	s_waitcnt lgkmcnt(0)
	v_mfma_f32_16x16x32_bf16 v[124:127], v[158:161], v[180:183], v[124:127]
	v_mfma_f32_16x16x32_bf16 v[120:123], v[172:175], v[180:183], v[120:123]
	v_mfma_f32_16x16x32_bf16 v[116:119], v[158:161], v[212:215], v[116:119]
	v_mfma_f32_16x16x32_bf16 v[112:115], v[172:175], v[212:215], v[112:115]
	v_mfma_f32_16x16x32_bf16 v[108:111], v[158:161], v[220:223], v[108:111]
	v_mfma_f32_16x16x32_bf16 v[104:107], v[172:175], v[220:223], v[104:107]
	v_mfma_f32_16x16x32_bf16 v[100:103], v[158:161], v[228:231], v[100:103]
	v_mfma_f32_16x16x32_bf16 v[96:99], v[172:175], v[228:231], v[96:99]
	v_mfma_f32_16x16x32_bf16 v[124:127], v[162:165], v[208:211], v[124:127]
	v_mfma_f32_16x16x32_bf16 v[120:123], v[176:179], v[208:211], v[120:123]
	v_mfma_f32_16x16x32_bf16 v[116:119], v[162:165], v[216:219], v[116:119]
	v_mfma_f32_16x16x32_bf16 v[112:115], v[176:179], v[216:219], v[112:115]
	v_mfma_f32_16x16x32_bf16 v[108:111], v[162:165], v[224:227], v[108:111]
	v_mfma_f32_16x16x32_bf16 v[104:107], v[176:179], v[224:227], v[104:107]
	v_mfma_f32_16x16x32_bf16 v[100:103], v[162:165], v[232:235], v[100:103]
	v_mfma_f32_16x16x32_bf16 v[96:99], v[176:179], v[232:235], v[96:99]
	s_barrier
	s_setprio 0
	s_add_i32 s38, 0, 0x1c000
	s_add_i32 s39, s58, s9
	v_add_u32_e32 v129, s38, v135
	v_lshl_add_u64 v[184:185], v[184:185], 0, s[94:95]
	s_mov_b32 m0, s39
	ds_read_b128 v[236:239], v129
	ds_read_b128 v[240:243], v129 offset:1024
	ds_read_b128 v[244:247], v129 offset:2048
	ds_read_b128 v[248:251], v129 offset:3072
	global_load_lds_dwordx4 v[184:185], off
	v_lshl_add_u64 v[184:185], v[188:189], 0, s[94:95]
	s_add_i32 m0, s39, 0x2000
	s_nop 0
	global_load_lds_dwordx4 v[184:185], off
	s_setprio 1
	s_barrier
	s_waitcnt lgkmcnt(0)
	v_mfma_f32_16x16x32_bf16 v[92:95], v[236:239], v[180:183], v[92:95]
	v_mfma_f32_16x16x32_bf16 v[88:91], v[244:247], v[180:183], v[88:91]
	ds_read_b128 v[180:183], v152 offset:49152
	v_mfma_f32_16x16x32_bf16 v[84:87], v[236:239], v[212:215], v[84:87]
	v_mfma_f32_16x16x32_bf16 v[80:83], v[244:247], v[212:215], v[80:83]
	ds_read_b128 v[212:215], v152 offset:51200
	v_mfma_f32_16x16x32_bf16 v[76:79], v[236:239], v[220:223], v[76:79]
	v_mfma_f32_16x16x32_bf16 v[72:75], v[244:247], v[220:223], v[72:75]
	ds_read_b128 v[220:223], v152 offset:53248
	v_mfma_f32_16x16x32_bf16 v[68:71], v[236:239], v[228:231], v[68:71]
	v_mfma_f32_16x16x32_bf16 v[64:67], v[244:247], v[228:231], v[64:67]
	ds_read_b128 v[228:231], v152 offset:55296
	v_mfma_f32_16x16x32_bf16 v[92:95], v[240:243], v[208:211], v[92:95]
	v_mfma_f32_16x16x32_bf16 v[88:91], v[248:251], v[208:211], v[88:91]
	ds_read_b128 v[208:211], v152 offset:50176
	v_mfma_f32_16x16x32_bf16 v[84:87], v[240:243], v[216:219], v[84:87]
	v_mfma_f32_16x16x32_bf16 v[80:83], v[248:251], v[216:219], v[80:83]
	ds_read_b128 v[216:219], v152 offset:52224
	v_mfma_f32_16x16x32_bf16 v[76:79], v[240:243], v[224:227], v[76:79]
	v_mfma_f32_16x16x32_bf16 v[72:75], v[248:251], v[224:227], v[72:75]
	ds_read_b128 v[224:227], v152 offset:54272
	v_mfma_f32_16x16x32_bf16 v[68:71], v[240:243], v[232:235], v[68:71]
	v_mfma_f32_16x16x32_bf16 v[64:67], v[248:251], v[232:235], v[64:67]
	ds_read_b128 v[232:235], v152 offset:56320
	s_barrier
	s_setprio 0
	s_mov_b32 m0, s47
	v_lshl_add_u64 v[170:171], v[170:171], 0, s[94:95]
	global_load_lds_dwordx4 v[170:171], off
	v_lshl_add_u64 v[166:167], v[166:167], 0, s[94:95]
	s_mov_b32 m0, s48
	s_nop 0
	global_load_lds_dwordx4 v[166:167], off
	s_waitcnt vmcnt(8)
	s_setprio 1
	s_barrier
	s_waitcnt lgkmcnt(0)
	v_mfma_f32_16x16x32_bf16 v[60:63], v[158:161], v[180:183], v[60:63]
	v_mfma_f32_16x16x32_bf16 v[56:59], v[172:175], v[180:183], v[56:59]
	v_mfma_f32_16x16x32_bf16 v[52:55], v[158:161], v[212:215], v[52:55]
	v_mfma_f32_16x16x32_bf16 v[48:51], v[172:175], v[212:215], v[48:51]
	v_mfma_f32_16x16x32_bf16 v[44:47], v[158:161], v[220:223], v[44:47]
	v_mfma_f32_16x16x32_bf16 v[40:43], v[172:175], v[220:223], v[40:43]
	v_mfma_f32_16x16x32_bf16 v[36:39], v[158:161], v[228:231], v[36:39]
	v_mfma_f32_16x16x32_bf16 v[32:35], v[172:175], v[228:231], v[32:35]
	v_mfma_f32_16x16x32_bf16 v[60:63], v[162:165], v[208:211], v[60:63]
	v_mfma_f32_16x16x32_bf16 v[56:59], v[176:179], v[208:211], v[56:59]
	v_mfma_f32_16x16x32_bf16 v[52:55], v[162:165], v[216:219], v[52:55]
	v_mfma_f32_16x16x32_bf16 v[48:51], v[176:179], v[216:219], v[48:51]
	v_mfma_f32_16x16x32_bf16 v[44:47], v[162:165], v[224:227], v[44:47]
	v_mfma_f32_16x16x32_bf16 v[40:43], v[176:179], v[224:227], v[40:43]
	v_mfma_f32_16x16x32_bf16 v[36:39], v[162:165], v[232:235], v[36:39]
	v_mfma_f32_16x16x32_bf16 v[32:35], v[176:179], v[232:235], v[32:35]
	s_barrier
	s_setprio 0
	s_add_u32 s36, s36, 0x80080
	s_addc_u32 s37, s37, 0
	s_add_i32 s38, s38, s9
	v_lshl_add_u64 v[158:159], s[36:37], 0, v[130:131]
	s_mov_b32 m0, s38
	s_nop 0
	global_load_lds_dwordx4 v[158:159], off
	v_lshl_add_u64 v[158:159], s[36:37], 0, v[136:137]
	s_add_i32 m0, s38, 0x2000
	s_nop 0
	global_load_lds_dwordx4 v[158:159], off
	s_waitcnt vmcnt(6)
	s_setprio 1
	s_barrier
	v_mfma_f32_16x16x32_bf16 v[28:31], v[236:239], v[180:183], v[28:31]
	v_mfma_f32_16x16x32_bf16 v[24:27], v[244:247], v[180:183], v[24:27]
	ds_read_b128 v[180:183], v152
	v_mfma_f32_16x16x32_bf16 v[20:23], v[236:239], v[212:215], v[20:23]
	v_mfma_f32_16x16x32_bf16 v[16:19], v[244:247], v[212:215], v[16:19]
	ds_read_b128 v[212:215], v152 offset:2048
	v_mfma_f32_16x16x32_bf16 v[12:15], v[236:239], v[220:223], v[12:15]
	v_mfma_f32_16x16x32_bf16 v[8:11], v[244:247], v[220:223], v[8:11]
	ds_read_b128 v[220:223], v152 offset:4096
	v_mfma_f32_16x16x32_bf16 v[4:7], v[236:239], v[228:231], v[4:7]
	v_mfma_f32_16x16x32_bf16 v[0:3], v[244:247], v[228:231], v[0:3]
	ds_read_b128 v[228:231], v152 offset:6144
	v_mfma_f32_16x16x32_bf16 v[28:31], v[240:243], v[208:211], v[28:31]
	v_mfma_f32_16x16x32_bf16 v[24:27], v[248:251], v[208:211], v[24:27]
	ds_read_b128 v[208:211], v152 offset:1024
	v_mfma_f32_16x16x32_bf16 v[20:23], v[240:243], v[216:219], v[20:23]
	v_mfma_f32_16x16x32_bf16 v[16:19], v[248:251], v[216:219], v[16:19]
	ds_read_b128 v[216:219], v152 offset:3072
	v_mfma_f32_16x16x32_bf16 v[12:15], v[240:243], v[224:227], v[12:15]
	v_mfma_f32_16x16x32_bf16 v[8:11], v[248:251], v[224:227], v[8:11]
	ds_read_b128 v[224:227], v152 offset:5120
	v_mfma_f32_16x16x32_bf16 v[4:7], v[240:243], v[232:235], v[4:7]
	v_mfma_f32_16x16x32_bf16 v[0:3], v[248:251], v[232:235], v[0:3]
	ds_read_b128 v[232:235], v152 offset:7168
	s_barrier
	s_setprio 0
	s_add_i32 s57, s57, 2
	s_add_u32 s34, s34, 0x100
	s_addc_u32 s35, s35, 0
	s_cmp_gt_u32 s57, 29
	s_cbranch_scc0 .LBB0_1423
	s_waitcnt lgkmcnt(0)
	s_and_b64 vcc, exec, s[16:17]
	s_cbranch_vccz .LBB0_1426
	s_barrier
